# P6: results transposed within lane quads through wave-private LDS so each store instruction writes complete 64-byte segments
# speedup vs baseline: 1.0475x; 1.0114x over previous
; __device__ __forceinline__ int otid() { int t = threadIdx.x; asm volatile("" : "+v"(t)); return t; }
; __device__ void phase6(const Params& p) {
;     const int tid_ = otid(); const int lane = tid_ & 63, wid = tid_ >> 6;
;     const int nw = gridDim.x * NWV;
;     int R = blockIdx.x * NWV + wid;
;     if (R >= NLAT) return;
;     uint4 ywn[8], xan, xbn, san, sbn; float4 gan, gbn;
;     ...
;     P6_LOAD(R);
;     int bcur = -1; float4 g2v[4];
;     for (;;) {
;         uint4 yw[8]; const uint4 xa = xan, xb = xbn, sa = san, sb = sbn; const float4 ga = gan, gb = gbn;
; #pragma unroll
;         for (int k = 0; k < 8; ++k) yw[k] = ywn[k];
;         const int Rn = R + nw; const bool more = Rn < NLAT;
;         if (more) P6_LOAD(Rn);
;         const int b = R >> 13;
;         if (b != bcur) { bcur = b;
; #pragma unroll
;             for (int q = 0; q < 4; ++q) g2v[q] = *(const float4*)(p.mod + b * 6144 + 5120 + lane * 16 + q * 4); }
;         const float gk[8] = {ga.x * 0.0625f, ga.y * 0.0625f, ga.z * 0.0625f, ga.w * 0.0625f, gb.x * 0.0625f, gb.y * 0.0625f, gb.z * 0.0625f, gb.w * 0.0625f};
;         float sacc[16];
; #pragma unroll
;         for (int j = 0; j < 16; ++j) sacc[j] = 0.f;
; #pragma unroll
;         for (int k = 0; k < 8; ++k) {
;             const unsigned wv[4] = {yw[k].x, yw[k].y, yw[k].z, yw[k].w};
; #pragma unroll
;             for (int q = 0; q < 4; ++q) {
;                 const f32v2 lo = __builtin_amdgcn_cvt_pk_f32_fp8((int)wv[q], false), hi = __builtin_amdgcn_cvt_pk_f32_fp8((int)wv[q], true);
;                 sacc[q * 4 + 0] += gk[k] * lo[0]; sacc[q * 4 + 1] += gk[k] * lo[1]; sacc[q * 4 + 2] += gk[k] * hi[0]; sacc[q * 4 + 3] += gk[k] * hi[1];
.LBB0_1289:
	s_or_b64 exec, exec, s[0:1]
	s_waitcnt lgkmcnt(0)
	s_barrier
	v_lshlrev_b32_e32 v246, 6, v0
	v_and_b32_e32 v247, 3, v0
	v_mul_u32_u24_e32 v252, 48, v247
	v_sub_u32_e32 v247, v246, v252
	v_sub_u32_e32 v252, 0, v252
	v_ashrrev_i32_e32 v253, 31, v252
	s_mov_b32 s22, 0x8000
	v_ashrrev_i32_e32 v1, 6, v0
	v_add_u32_e32 v138, s81, v1
	v_cmp_gt_i32_e32 vcc, s22, v138
	s_and_saveexec_b64 s[0:1], vcc
	s_cbranch_execz .LBB0_1296
	v_ashrrev_i32_e32 v139, 31, v138
	v_lshlrev_b64 v[2:3], 13, v[138:139]
	v_lshlrev_b32_e32 v1, 4, v0
	v_lshl_add_u64 v[2:3], s[50:51], 0, v[2:3]
	v_and_b32_e32 v130, 0x3f0, v1
	v_mov_b32_e32 v131, 0
	v_lshl_add_u64 v[2:3], v[2:3], 0, v[130:131]
	s_movk_i32 s0, 0x1000
	global_load_dwordx4 v[62:65], v[2:3], off
	global_load_dwordx4 v[58:61], v[2:3], off offset:1024
	global_load_dwordx4 v[54:57], v[2:3], off offset:2048
	global_load_dwordx4 v[46:49], v[2:3], off offset:3072
	v_add_co_u32_e32 v2, vcc, s0, v2
	v_lshlrev_b64 v[6:7], 11, v[138:139]
	s_nop 0
	v_addc_co_u32_e32 v3, vcc, 0, v3, vcc
	global_load_dwordx4 v[50:53], v[2:3], off
	global_load_dwordx4 v[42:45], v[2:3], off offset:1024
	global_load_dwordx4 v[38:41], v[2:3], off offset:2048
	global_load_dwordx4 v[34:37], v[2:3], off offset:3072
	v_lshl_add_u64 v[2:3], s[24:25], 0, v[6:7]
	v_lshlrev_b32_e32 v8, 1, v130
	v_mov_b32_e32 v9, v131
	v_lshl_add_u64 v[10:11], v[2:3], 0, v[8:9]
	v_lshl_add_u64 v[6:7], s[26:27], 0, v[6:7]
	global_load_dwordx4 v[2:5], v[10:11], off offset:16
	global_load_dwordx4 v[26:29], v[10:11], off
	v_lshl_add_u64 v[10:11], v[6:7], 0, v[8:9]
	global_load_dwordx4 v[6:9], v[10:11], off offset:16
	global_load_dwordx4 v[30:33], v[10:11], off
	v_lshlrev_b64 v[10:11], 5, v[138:139]
	v_lshl_add_u64 v[10:11], s[36:37], 0, v[10:11]
	global_load_dwordx4 v[114:117], v[10:11], off offset:16
	global_load_dwordx4 v[118:121], v[10:11], off
	v_lshlrev_b64 v[10:11], 12, v[138:139]
	v_and_b32_e32 v12, 63, v0
	v_lshl_or_b32 v10, v12, 6, v10
	v_lshl_add_u64 v[0:1], s[88:89], 0, v[10:11]
	v_add_u32_e32 v10, s82, v138
	v_ashrrev_i32_e32 v11, 31, v10
	s_ashr_i32 s83, s82, 31
	v_lshlrev_b64 v[134:135], 11, v[10:11]
	v_lshlrev_b64 v[136:137], 13, v[10:11]
	s_lshl_b64 s[2:3], s[82:83], 12
	v_lshlrev_b64 v[132:133], 5, v[10:11]
	s_lshl_b64 s[4:5], s[82:83], 5
	v_lshl_or_b32 v134, v12, 5, v134
	s_lshl_b64 s[6:7], s[82:83], 11
	v_or_b32_e32 v136, v136, v130
	s_lshl_b64 s[8:9], s[82:83], 13
	v_mov_b32_e32 v139, -1
	s_mov_b64 s[10:11], 0
	s_movk_i32 s23, 0x7fff
	s_mov_b32 s24, 0x17de8000
	s_mov_b32 s25, 0x17de9000
	s_mov_b64 s[12:13], 0x13de7600
	s_mov_b32 s26, 0x13de7000
	s_mov_b64 s[14:15], 0xce7600
	s_mov_b32 s27, 0xce7000
	s_mov_b64 s[16:17], 0x4ce7600
	v_lshlrev_b32_e32 v130, 2, v130
	s_mov_b64 s[18:19], 0x5000
	s_branch .LBB0_1292
.LBB0_1291:
	s_or_b64 exec, exec, s[20:21]
	v_cvt_pk_f32_fp8_e32 v[146:147], v62
	v_cvt_pk_f32_fp8_e32 v[158:159], v58
	v_cvt_pk_f32_fp8_e32 v[170:171], v54
	v_mul_f32_e32 v118, 0x3d800000, v118
	v_cvt_pk_f32_fp8_e32 v[182:183], v46
	v_mul_f32_e32 v138, 0x3d800000, v119
	v_cvt_pk_f32_fp8_e32 v[194:195], v50
	v_pk_fma_f32 v[146:147], v[118:119], v[146:147], 0 op_sel_hi:[0,1,0]
	v_mul_f32_e32 v120, 0x3d800000, v120
	v_cvt_pk_f32_fp8_e32 v[206:207], v42
	v_pk_fma_f32 v[146:147], v[138:139], v[158:159], v[146:147] op_sel_hi:[0,1,1]
	v_mul_f32_e32 v140, 0x3d800000, v121
	v_cvt_pk_f32_fp8_e32 v[218:219], v38
	v_pk_fma_f32 v[146:147], v[120:121], v[170:171], v[146:147] op_sel_hi:[0,1,1]
	v_mul_f32_e32 v114, 0x3d800000, v114
	v_cvt_pk_f32_fp8_e32 v[230:231], v34
	v_pk_fma_f32 v[146:147], v[140:141], v[182:183], v[146:147] op_sel_hi:[0,1,1]
	v_mul_f32_e32 v142, 0x3d800000, v115
	v_pk_fma_f32 v[146:147], v[114:115], v[194:195], v[146:147] op_sel_hi:[0,1,1]
	v_mul_f32_e32 v116, 0x3d800000, v116
	v_cvt_pk_f32_fp8_sdwa v[148:149], v62 src0_sel:WORD_1
	v_pk_fma_f32 v[146:147], v[142:143], v[206:207], v[146:147] op_sel_hi:[0,1,1]
	v_mul_f32_e32 v144, 0x3d800000, v117
	v_cvt_pk_f32_fp8_sdwa v[160:161], v58 src0_sel:WORD_1
	v_pk_fma_f32 v[146:147], v[116:117], v[218:219], v[146:147] op_sel_hi:[0,1,1]
	v_cvt_pk_f32_fp8_sdwa v[172:173], v54 src0_sel:WORD_1
	v_cvt_pk_f32_fp8_e32 v[238:239], v36
	v_cvt_pk_f32_fp8_sdwa v[240:241], v36 src0_sel:WORD_1
	v_cvt_pk_f32_fp8_e32 v[242:243], v37
	v_cvt_pk_f32_fp8_sdwa v[244:245], v37 src0_sel:WORD_1
	v_lshlrev_b32_e32 v36, 16, v30
	v_and_b32_e32 v37, 0xffff0000, v30
	v_pk_fma_f32 v[146:147], v[144:145], v[230:231], v[146:147] op_sel_hi:[0,1,1]
	v_cvt_pk_f32_fp8_sdwa v[184:185], v46 src0_sel:WORD_1
	v_cvt_pk_f32_fp8_sdwa v[232:233], v34 src0_sel:WORD_1
	v_cvt_pk_f32_fp8_e32 v[234:235], v35
	v_cvt_pk_f32_fp8_sdwa v[236:237], v35 src0_sel:WORD_1
	v_lshlrev_b32_e32 v34, 16, v26
	v_and_b32_e32 v35, 0xffff0000, v26
	v_pk_add_f32 v[36:37], v[146:147], v[36:37]
	v_cvt_pk_f32_fp8_sdwa v[196:197], v50 src0_sel:WORD_1
	s_waitcnt vmcnt(3)
; __device__ void phase6(const Params& p) {
;     ...
;         for (int k = 0; k < 8; ++k) {
;             const unsigned wv[4] = {yw[k].x, yw[k].y, yw[k].z, yw[k].w};
; #pragma unroll
;             for (int q = 0; q < 4; ++q) {
;                 const f32v2 lo = __builtin_amdgcn_cvt_pk_f32_fp8((int)wv[q], false), hi = __builtin_amdgcn_cvt_pk_f32_fp8((int)wv[q], true);
;                 sacc[q * 4 + 0] += gk[k] * lo[0]; sacc[q * 4 + 1] += gk[k] * lo[1]; sacc[q * 4 + 2] += gk[k] * hi[0]; sacc[q * 4 + 3] += gk[k] * hi[1];
;             }
;         }
;         const unsigned xw[8] = {xa.x, xa.y, xa.z, xa.w, xb.x, xb.y, xb.z, xb.w}, sw[8] = {sa.x, sa.y, sa.z, sa.w, sb.x, sb.y, sb.z, sb.w};
; #pragma unroll
;         for (int q = 0; q < 4; ++q) {
;             const int col = lane * 16 + q * 4;
;             const float4 g2 = g2v[q];
;             float4 r;
;             r.x = __uint_as_float(xw[q * 2] << 16) + g2.x * (sacc[q * 4 + 0] + __uint_as_float(sw[q * 2] << 16));
;             r.y = __uint_as_float(xw[q * 2] & 0xffff0000u) + g2.y * (sacc[q * 4 + 1] + __uint_as_float(sw[q * 2] & 0xffff0000u));
;             r.z = __uint_as_float(xw[q * 2 + 1] << 16) + g2.z * (sacc[q * 4 + 2] + __uint_as_float(sw[q * 2 + 1] << 16));
;             r.w = __uint_as_float(xw[q * 2 + 1] & 0xffff0000u) + g2.w * (sacc[q * 4 + 3] + __uint_as_float(sw[q * 2 + 1] & 0xffff0000u));
;             *(float4*)(p.out + (size_t)R * D + col) = r;
	v_pk_fma_f32 v[34:35], v[10:11], v[36:37], v[34:35]
	v_pk_fma_f32 v[36:37], v[118:119], v[148:149], 0 op_sel_hi:[0,1,0]
	v_cvt_pk_f32_fp8_sdwa v[208:209], v42 src0_sel:WORD_1
	v_pk_fma_f32 v[36:37], v[138:139], v[160:161], v[36:37] op_sel_hi:[0,1,1]
	v_cvt_pk_f32_fp8_sdwa v[220:221], v38 src0_sel:WORD_1
	v_pk_fma_f32 v[36:37], v[120:121], v[172:173], v[36:37] op_sel_hi:[0,1,1]
	v_pk_fma_f32 v[36:37], v[140:141], v[184:185], v[36:37] op_sel_hi:[0,1,1]
	v_pk_fma_f32 v[36:37], v[114:115], v[196:197], v[36:37] op_sel_hi:[0,1,1]
	v_pk_fma_f32 v[36:37], v[142:143], v[208:209], v[36:37] op_sel_hi:[0,1,1]
	v_cvt_pk_f32_fp8_e32 v[150:151], v63
	v_pk_fma_f32 v[36:37], v[116:117], v[220:221], v[36:37] op_sel_hi:[0,1,1]
	v_cvt_pk_f32_fp8_e32 v[162:163], v59
	v_lshlrev_b32_e32 v30, 16, v31
	v_and_b32_e32 v31, 0xffff0000, v31
	v_pk_fma_f32 v[36:37], v[144:145], v[232:233], v[36:37] op_sel_hi:[0,1,1]
	v_cvt_pk_f32_fp8_e32 v[174:175], v55
	v_lshlrev_b32_e32 v26, 16, v27
	v_and_b32_e32 v27, 0xffff0000, v27
	v_pk_add_f32 v[30:31], v[36:37], v[30:31]
	v_cvt_pk_f32_fp8_e32 v[186:187], v47
	v_pk_fma_f32 v[36:37], v[12:13], v[30:31], v[26:27]
	v_cvt_pk_f32_fp8_e32 v[198:199], v51
	ds_write_b128 v246, v[34:37]
	v_cvt_pk_f32_fp8_e32 v[210:211], v43
	v_cvt_pk_f32_fp8_e32 v[222:223], v39
	v_pk_fma_f32 v[34:35], v[118:119], v[150:151], 0 op_sel_hi:[0,1,0]
	v_pk_fma_f32 v[34:35], v[138:139], v[162:163], v[34:35] op_sel_hi:[0,1,1]
	v_pk_fma_f32 v[34:35], v[120:121], v[174:175], v[34:35] op_sel_hi:[0,1,1]
	v_pk_fma_f32 v[34:35], v[140:141], v[186:187], v[34:35] op_sel_hi:[0,1,1]
	v_pk_fma_f32 v[34:35], v[114:115], v[198:199], v[34:35] op_sel_hi:[0,1,1]
	v_cvt_pk_f32_fp8_sdwa v[62:63], v63 src0_sel:WORD_1
	v_pk_fma_f32 v[34:35], v[142:143], v[210:211], v[34:35] op_sel_hi:[0,1,1]
	v_cvt_pk_f32_fp8_sdwa v[58:59], v59 src0_sel:WORD_1
	v_pk_fma_f32 v[34:35], v[116:117], v[222:223], v[34:35] op_sel_hi:[0,1,1]
	v_cvt_pk_f32_fp8_sdwa v[54:55], v55 src0_sel:WORD_1
	v_lshlrev_b32_e32 v30, 16, v32
	v_and_b32_e32 v31, 0xffff0000, v32
	v_pk_fma_f32 v[34:35], v[144:145], v[234:235], v[34:35] op_sel_hi:[0,1,1]
	v_cvt_pk_f32_fp8_sdwa v[46:47], v47 src0_sel:WORD_1
	v_lshlrev_b32_e32 v26, 16, v28
	v_and_b32_e32 v27, 0xffff0000, v28
	v_pk_add_f32 v[30:31], v[34:35], v[30:31]
	v_cvt_pk_f32_fp8_sdwa v[50:51], v51 src0_sel:WORD_1
	s_waitcnt vmcnt(0)
	v_pk_fma_f32 v[26:27], v[14:15], v[30:31], v[26:27]
	v_pk_fma_f32 v[30:31], v[118:119], v[62:63], 0 op_sel_hi:[0,1,0]
	v_cvt_pk_f32_fp8_sdwa v[42:43], v43 src0_sel:WORD_1
	v_pk_fma_f32 v[30:31], v[138:139], v[58:59], v[30:31] op_sel_hi:[0,1,1]
	v_cvt_pk_f32_fp8_sdwa v[38:39], v39 src0_sel:WORD_1
	v_pk_fma_f32 v[30:31], v[120:121], v[54:55], v[30:31] op_sel_hi:[0,1,1]
	v_pk_fma_f32 v[30:31], v[140:141], v[46:47], v[30:31] op_sel_hi:[0,1,1]
	v_pk_fma_f32 v[30:31], v[114:115], v[50:51], v[30:31] op_sel_hi:[0,1,1]
	v_cvt_pk_f32_fp8_e32 v[152:153], v64
	v_pk_fma_f32 v[30:31], v[142:143], v[42:43], v[30:31] op_sel_hi:[0,1,1]
	v_cvt_pk_f32_fp8_e32 v[164:165], v60
	v_pk_fma_f32 v[30:31], v[116:117], v[38:39], v[30:31] op_sel_hi:[0,1,1]
	v_cvt_pk_f32_fp8_e32 v[176:177], v56
	v_lshlrev_b32_e32 v32, 16, v33
	v_and_b32_e32 v33, 0xffff0000, v33
	v_pk_fma_f32 v[30:31], v[144:145], v[236:237], v[30:31] op_sel_hi:[0,1,1]
	v_cvt_pk_f32_fp8_e32 v[188:189], v48
	v_lshlrev_b32_e32 v28, 16, v29
	v_and_b32_e32 v29, 0xffff0000, v29
	v_pk_add_f32 v[30:31], v[30:31], v[32:33]
	v_cvt_pk_f32_fp8_e32 v[200:201], v52
	v_pk_fma_f32 v[28:29], v[16:17], v[30:31], v[28:29]
	v_pk_fma_f32 v[30:31], v[118:119], v[152:153], 0 op_sel_hi:[0,1,0]
	v_cvt_pk_f32_fp8_e32 v[212:213], v44
	v_pk_fma_f32 v[30:31], v[138:139], v[164:165], v[30:31] op_sel_hi:[0,1,1]
	v_cvt_pk_f32_fp8_e32 v[224:225], v40
	v_pk_fma_f32 v[30:31], v[120:121], v[176:177], v[30:31] op_sel_hi:[0,1,1]
	v_pk_fma_f32 v[30:31], v[140:141], v[188:189], v[30:31] op_sel_hi:[0,1,1]
	v_pk_fma_f32 v[30:31], v[114:115], v[200:201], v[30:31] op_sel_hi:[0,1,1]
	v_cvt_pk_f32_fp8_sdwa v[154:155], v64 src0_sel:WORD_1
	v_pk_fma_f32 v[30:31], v[142:143], v[212:213], v[30:31] op_sel_hi:[0,1,1]
	v_cvt_pk_f32_fp8_sdwa v[166:167], v60 src0_sel:WORD_1
	v_pk_fma_f32 v[30:31], v[116:117], v[224:225], v[30:31] op_sel_hi:[0,1,1]
	v_cvt_pk_f32_fp8_sdwa v[178:179], v56 src0_sel:WORD_1
	ds_write_b128 v246, v[26:29] offset:16
	v_pk_fma_f32 v[30:31], v[144:145], v[238:239], v[30:31] op_sel_hi:[0,1,1]
	v_cvt_pk_f32_fp8_sdwa v[190:191], v48 src0_sel:WORD_1
	v_lshlrev_b32_e32 v28, 16, v6
	v_and_b32_e32 v29, 0xffff0000, v6
	v_lshlrev_b32_e32 v26, 16, v2
	v_and_b32_e32 v27, 0xffff0000, v2
	v_pk_add_f32 v[28:29], v[30:31], v[28:29]
	v_cvt_pk_f32_fp8_sdwa v[202:203], v52 src0_sel:WORD_1
	v_pk_fma_f32 v[26:27], v[18:19], v[28:29], v[26:27]
	v_pk_fma_f32 v[28:29], v[118:119], v[154:155], 0 op_sel_hi:[0,1,0]
	v_cvt_pk_f32_fp8_sdwa v[214:215], v44 src0_sel:WORD_1
; __device__ void phase6(const Params& p) {
;     ...
;         const unsigned xw[8] = {xa.x, xa.y, xa.z, xa.w, xb.x, xb.y, xb.z, xb.w}, sw[8] = {sa.x, sa.y, sa.z, sa.w, sb.x, sb.y, sb.z, sb.w};
; #pragma unroll
;         for (int q = 0; q < 4; ++q) {
;             const int col = lane * 16 + q * 4;
;             const float4 g2 = g2v[q];
;             float4 r;
;             r.x = __uint_as_float(xw[q * 2] << 16) + g2.x * (sacc[q * 4 + 0] + __uint_as_float(sw[q * 2] << 16));
;             r.y = __uint_as_float(xw[q * 2] & 0xffff0000u) + g2.y * (sacc[q * 4 + 1] + __uint_as_float(sw[q * 2] & 0xffff0000u));
;             r.z = __uint_as_float(xw[q * 2 + 1] << 16) + g2.z * (sacc[q * 4 + 2] + __uint_as_float(sw[q * 2 + 1] << 16));
;             r.w = __uint_as_float(xw[q * 2 + 1] & 0xffff0000u) + g2.w * (sacc[q * 4 + 3] + __uint_as_float(sw[q * 2 + 1] & 0xffff0000u));
;             *(float4*)(p.out + (size_t)R * D + col) = r;
;         }
;         if (!more) break;
;         R = Rn;
	v_pk_fma_f32 v[28:29], v[138:139], v[166:167], v[28:29] op_sel_hi:[0,1,1]
	v_cvt_pk_f32_fp8_sdwa v[226:227], v40 src0_sel:WORD_1
	v_pk_fma_f32 v[28:29], v[120:121], v[178:179], v[28:29] op_sel_hi:[0,1,1]
	v_pk_fma_f32 v[28:29], v[140:141], v[190:191], v[28:29] op_sel_hi:[0,1,1]
	v_pk_fma_f32 v[28:29], v[114:115], v[202:203], v[28:29] op_sel_hi:[0,1,1]
	v_pk_fma_f32 v[28:29], v[142:143], v[214:215], v[28:29] op_sel_hi:[0,1,1]
	v_cvt_pk_f32_fp8_e32 v[156:157], v65
	v_pk_fma_f32 v[28:29], v[116:117], v[226:227], v[28:29] op_sel_hi:[0,1,1]
	v_cvt_pk_f32_fp8_e32 v[168:169], v61
	v_lshlrev_b32_e32 v6, 16, v7
	v_and_b32_e32 v7, 0xffff0000, v7
	v_pk_fma_f32 v[28:29], v[144:145], v[240:241], v[28:29] op_sel_hi:[0,1,1]
	v_cvt_pk_f32_fp8_e32 v[180:181], v57
	v_lshlrev_b32_e32 v2, 16, v3
	v_and_b32_e32 v3, 0xffff0000, v3
	v_pk_add_f32 v[6:7], v[28:29], v[6:7]
	v_cvt_pk_f32_fp8_e32 v[192:193], v49
	v_pk_fma_f32 v[28:29], v[20:21], v[6:7], v[2:3]
	v_cvt_pk_f32_fp8_e32 v[204:205], v53
	ds_write_b128 v246, v[26:29] offset:32
	v_cvt_pk_f32_fp8_e32 v[216:217], v45
	v_cvt_pk_f32_fp8_e32 v[228:229], v41
	v_pk_fma_f32 v[26:27], v[118:119], v[156:157], 0 op_sel_hi:[0,1,0]
	v_pk_fma_f32 v[26:27], v[138:139], v[168:169], v[26:27] op_sel_hi:[0,1,1]
	v_pk_fma_f32 v[26:27], v[120:121], v[180:181], v[26:27] op_sel_hi:[0,1,1]
	v_pk_fma_f32 v[26:27], v[140:141], v[192:193], v[26:27] op_sel_hi:[0,1,1]
	v_pk_fma_f32 v[26:27], v[114:115], v[204:205], v[26:27] op_sel_hi:[0,1,1]
	v_cvt_pk_f32_fp8_sdwa v[64:65], v65 src0_sel:WORD_1
	v_pk_fma_f32 v[26:27], v[142:143], v[216:217], v[26:27] op_sel_hi:[0,1,1]
	v_cvt_pk_f32_fp8_sdwa v[60:61], v61 src0_sel:WORD_1
	v_pk_fma_f32 v[26:27], v[116:117], v[228:229], v[26:27] op_sel_hi:[0,1,1]
	v_cvt_pk_f32_fp8_sdwa v[56:57], v57 src0_sel:WORD_1
	v_lshlrev_b32_e32 v6, 16, v8
	v_and_b32_e32 v7, 0xffff0000, v8
	v_pk_fma_f32 v[26:27], v[144:145], v[242:243], v[26:27] op_sel_hi:[0,1,1]
	v_cvt_pk_f32_fp8_sdwa v[48:49], v49 src0_sel:WORD_1
	v_lshlrev_b32_e32 v2, 16, v4
	v_and_b32_e32 v3, 0xffff0000, v4
	v_pk_add_f32 v[6:7], v[26:27], v[6:7]
	v_cvt_pk_f32_fp8_sdwa v[52:53], v53 src0_sel:WORD_1
	v_pk_fma_f32 v[2:3], v[22:23], v[6:7], v[2:3]
	v_pk_fma_f32 v[6:7], v[118:119], v[64:65], 0 op_sel_hi:[0,1,0]
	v_cvt_pk_f32_fp8_sdwa v[44:45], v45 src0_sel:WORD_1
	v_pk_fma_f32 v[6:7], v[138:139], v[60:61], v[6:7] op_sel_hi:[0,1,1]
	v_cvt_pk_f32_fp8_sdwa v[40:41], v41 src0_sel:WORD_1
	v_pk_fma_f32 v[6:7], v[120:121], v[56:57], v[6:7] op_sel_hi:[0,1,1]
	v_pk_fma_f32 v[6:7], v[140:141], v[48:49], v[6:7] op_sel_hi:[0,1,1]
	v_pk_fma_f32 v[6:7], v[114:115], v[52:53], v[6:7] op_sel_hi:[0,1,1]
	v_pk_fma_f32 v[6:7], v[142:143], v[44:45], v[6:7] op_sel_hi:[0,1,1]
	v_pk_fma_f32 v[6:7], v[116:117], v[40:41], v[6:7] op_sel_hi:[0,1,1]
	v_lshlrev_b32_e32 v8, 16, v9
	v_and_b32_e32 v9, 0xffff0000, v9
	v_pk_fma_f32 v[6:7], v[144:145], v[244:245], v[6:7] op_sel_hi:[0,1,1]
	v_lshlrev_b32_e32 v4, 16, v5
	v_and_b32_e32 v5, 0xffff0000, v5
	v_pk_add_f32 v[6:7], v[6:7], v[8:9]
	s_and_b64 s[0:1], exec, s[0:1]
	v_pk_fma_f32 v[4:5], v[24:25], v[6:7], v[4:5]
	s_or_b64 s[10:11], s[0:1], s[10:11]
	ds_write_b128 v246, v[2:5] offset:48
	s_waitcnt lgkmcnt(0)
	ds_read_b128 v[2:5], v247
	ds_read_b128 v[6:9], v247 offset:64
	ds_read_b128 v[26:29], v247 offset:128
	ds_read_b128 v[30:33], v247 offset:192
	v_lshl_add_u64 v[254:255], v[0:1], 0, v[252:253]
	s_waitcnt lgkmcnt(0)
	global_store_dwordx4 v[254:255], v[2:5], off
	global_store_dwordx4 v[254:255], v[6:9], off offset:64
	global_store_dwordx4 v[254:255], v[26:29], off offset:128
	global_store_dwordx4 v[254:255], v[30:33], off offset:192
	v_lshl_add_u64 v[0:1], v[0:1], 0, s[2:3]
	v_lshl_add_u64 v[132:133], v[132:133], 0, s[4:5]
	v_lshl_add_u64 v[134:135], v[134:135], 0, s[6:7]
	v_lshl_add_u64 v[136:137], v[136:137], 0, s[8:9]
	v_mov_b32_e32 v138, v141
	v_mov_b64_e32 v[114:115], v[126:127]
	v_mov_b64_e32 v[116:117], v[128:129]
	v_mov_b64_e32 v[118:119], v[122:123]
	v_mov_b64_e32 v[120:121], v[124:125]
	v_mov_b64_e32 v[62:63], v[66:67]
	v_mov_b64_e32 v[64:65], v[68:69]
	v_mov_b64_e32 v[58:59], v[70:71]
	v_mov_b64_e32 v[60:61], v[72:73]
	v_mov_b64_e32 v[54:55], v[74:75]
	v_mov_b64_e32 v[56:57], v[76:77]
	v_mov_b64_e32 v[46:47], v[78:79]
	v_mov_b64_e32 v[48:49], v[80:81]
	v_mov_b64_e32 v[50:51], v[82:83]
	v_mov_b64_e32 v[52:53], v[84:85]
	v_mov_b64_e32 v[42:43], v[86:87]
	v_mov_b64_e32 v[44:45], v[88:89]
	v_mov_b64_e32 v[38:39], v[90:91]
	v_mov_b64_e32 v[40:41], v[92:93]
	v_mov_b64_e32 v[34:35], v[94:95]
	v_mov_b64_e32 v[36:37], v[96:97]
	v_mov_b64_e32 v[6:7], v[110:111]
	v_mov_b64_e32 v[8:9], v[112:113]
	v_mov_b64_e32 v[30:31], v[106:107]
	v_mov_b64_e32 v[32:33], v[108:109]
	v_mov_b64_e32 v[2:3], v[102:103]
	v_mov_b64_e32 v[4:5], v[104:105]
	v_mov_b64_e32 v[26:27], v[98:99]
	v_mov_b64_e32 v[28:29], v[100:101]
	s_andn2_b64 exec, exec, s[10:11]
	s_cbranch_execz .LBB0_1296
